# layer-0 RMSNorm loops: gain loaded once, all row loads issued together (was ~11 serialized round trips per row)
# speedup vs baseline: 1.0102x; 1.0048x over previous
; __device__ __forceinline__ unsigned pk2(float lo, float hi) { return f2bf(lo) | (f2bf(hi) << 16); }
; __device__ __forceinline__ float rms_row_load(const float* xrow, int lane, f32x4 (&v)[8]) {
;     const f32x4* xr = (const f32x4*)xrow + lane; float s = 0.f;
; #pragma unroll
;     for (int j = 0; j < 8; ++j) { v[j] = xr[64 * j]; s += (v[j].x * v[j].x + v[j].y * v[j].y) + (v[j].z * v[j].z + v[j].w * v[j].w); }
;     return 1.0f / sqrtf(wave_sum(s) * (1.0f / D) + EPS);
; }
; __device__ __forceinline__ void rms_row_to_bf16(const float* xrow, const float* gain, bf16* orow, int lane) {
;     f32x4 v[8]; const float rstd = rms_row_load(xrow, lane, v);
;     const f32x4* gr = (const f32x4*)gain + lane; unsigned long long* o8 = (unsigned long long*)orow + lane;
; #pragma unroll
;     for (int j = 0; j < 8; ++j) { const f32x4 g = gr[64 * j]; o8[64 * j] = (unsigned long long)pk2(v[j].x * rstd * g.x, v[j].y * rstd * g.y) | ((unsigned long long)pk2(v[j].z * rstd * g.z, v[j].w * rstd * g.w) << 32); }
; }
; __global__ void __launch_bounds__(NWAVES * 64, 2) trunk_fwd(Args args) {
;     ...
;             if (layer == 0) { for (int m = gw; m < M; m += ngw) rms_row_to_bf16(XA + (size_t)m * D, gain, Hb + (size_t)m * D, lane); }
.LBB0_777:
	s_and_b64 vcc, exec, s[0:1]
	s_cbranch_vccz .LBB0_781
	v_readlane_b32 s0, v250, 5
	s_add_i32 s4, s22, s0
	s_cmpk_gt_i32 s4, 0x1fff
	s_cbranch_scc1 .LBB0_781
	v_and_b32_e32 v2, 64, v228
	v_add_u32_e32 v2, 64, v2
	v_xor_b32_e32 v3, 1, v228
	v_cmp_lt_i32_e32 vcc, v3, v2
	v_lshlrev_b32_e32 v186, 4, v1
	v_lshl_add_u64 v[34:35], s[12:13], 0, v[186:187]
	v_cndmask_b32_e32 v3, v228, v3, vcc
	v_lshlrev_b32_e32 v50, 2, v3
	v_xor_b32_e32 v3, 2, v228
	v_cmp_lt_i32_e32 vcc, v3, v2
	s_mov_b64 s[0:1], 0x1000
	v_lshl_add_u64 v[36:37], v[34:35], 0, s[0:1]
	v_cndmask_b32_e32 v3, v228, v3, vcc
	v_lshlrev_b32_e32 v51, 2, v3
	v_xor_b32_e32 v3, 4, v228
	v_cmp_lt_i32_e32 vcc, v3, v2
	s_mov_b64 s[0:1], 0x1400
	v_lshl_add_u64 v[38:39], v[34:35], 0, s[0:1]
	v_cndmask_b32_e32 v3, v228, v3, vcc
	v_lshlrev_b32_e32 v52, 2, v3
	v_xor_b32_e32 v3, 8, v228
	v_cmp_lt_i32_e32 vcc, v3, v2
	s_mov_b64 s[0:1], 0x1800
	v_lshl_add_u64 v[40:41], v[34:35], 0, s[0:1]
	v_cndmask_b32_e32 v3, v228, v3, vcc
	v_lshlrev_b32_e32 v53, 2, v3
	v_xor_b32_e32 v3, 16, v228
	v_cmp_lt_i32_e32 vcc, v3, v2
	s_mov_b64 s[0:1], 0x1c00
	s_ashr_i32 s5, s4, 31
	v_cndmask_b32_e32 v3, v228, v3, vcc
	v_lshlrev_b32_e32 v54, 2, v3
	v_xor_b32_e32 v3, 32, v228
	v_cmp_lt_i32_e32 vcc, v3, v2
	v_lshl_add_u64 v[42:43], v[34:35], 0, s[0:1]
	s_lshl_b64 s[0:1], s[4:5], 12
	v_readlane_b32 s8, v254, 59
	v_cndmask_b32_e32 v2, v228, v3, vcc
	v_lshl_or_b32 v44, v1, 3, s0
	v_mov_b32_e32 v45, s1
	s_lshl_b64 s[0:1], s[4:5], 13
	v_readlane_b32 s6, v250, 6
	v_readlane_b32 s9, v254, 60
	v_readlane_b32 s14, v254, 57
	v_readlane_b32 s16, v254, 61
	v_lshlrev_b32_e32 v55, 2, v2
	v_or_b32_e32 v46, s0, v186
	v_mov_b32_e32 v47, s1
	v_readlane_b32 s7, v250, 7
	s_mov_b32 s5, 0xf800000
	s_mov_b32 s9, 0x36da2000
	s_mov_b32 s12, 0x34da1000
	v_readlane_b32 s15, v254, 58
	v_readlane_b32 s17, v254, 62
	global_load_dwordx4 v[60:63], v[34:35], off
	global_load_dwordx4 v[64:67], v[34:35], off offset:1024
	global_load_dwordx4 v[68:71], v[34:35], off offset:2048
	global_load_dwordx4 v[72:75], v[34:35], off offset:3072
	global_load_dwordx4 v[76:79], v[36:37], off
	global_load_dwordx4 v[80:83], v[38:39], off
	global_load_dwordx4 v[84:87], v[40:41], off
	global_load_dwordx4 v[88:91], v[42:43], off
.LBB0_780:
	v_lshl_add_u64 v[2:3], s[6:7], 0, v[46:47]
	v_add_co_u32_e32 v4, vcc, 0x36da1000, v2
	s_add_i32 s4, s4, s8
	s_nop 0
	v_addc_co_u32_e32 v5, vcc, 0, v3, vcc
	global_load_dwordx4 v[30:33], v[4:5], off
	global_load_dwordx4 v[26:29], v[4:5], off offset:1024
	global_load_dwordx4 v[22:25], v[4:5], off offset:2048
	global_load_dwordx4 v[18:21], v[4:5], off offset:3072
	v_add_co_u32_e32 v2, vcc, s9, v2
	v_lshl_add_u64 v[46:47], v[46:47], 0, s[16:17]
	s_nop 0
	v_addc_co_u32_e32 v3, vcc, 0, v3, vcc
	global_load_dwordx4 v[14:17], v[2:3], off
	global_load_dwordx4 v[10:13], v[2:3], off offset:1024
	global_load_dwordx4 v[6:9], v[2:3], off offset:2048
	global_load_dwordx4 v[2:5], v[2:3], off offset:3072
	s_cmpk_gt_i32 s4, 0x1fff
	v_lshl_add_u64 v[48:49], s[6:7], 0, v[44:45]
	v_add_co_u32_e32 v48, vcc, s12, v48
	s_nop 1
	v_addc_co_u32_e32 v49, vcc, 0, v49, vcc
	v_lshl_add_u64 v[44:45], v[44:45], 0, s[14:15]
	s_waitcnt vmcnt(7)
	v_mul_f32_e32 v1, v31, v31
	v_mul_f32_e32 v57, v33, v33
	v_fmac_f32_e32 v1, v30, v30
	v_fmac_f32_e32 v57, v32, v32
	v_add_f32_e32 v1, v1, v57
	s_waitcnt vmcnt(6)
	v_mul_f32_e32 v56, v27, v27
	v_mul_f32_e32 v57, v29, v29
	v_fmac_f32_e32 v56, v26, v26
	v_fmac_f32_e32 v57, v28, v28
	v_add_f32_e32 v56, v56, v57
	v_add_f32_e32 v1, v1, v56
	s_waitcnt vmcnt(5)
	v_mul_f32_e32 v56, v23, v23
	v_mul_f32_e32 v57, v25, v25
	v_fmac_f32_e32 v56, v22, v22
	v_fmac_f32_e32 v57, v24, v24
	v_add_f32_e32 v56, v56, v57
	v_add_f32_e32 v1, v1, v56
	s_waitcnt vmcnt(4)
	v_mul_f32_e32 v56, v19, v19
	v_mul_f32_e32 v57, v21, v21
	v_fmac_f32_e32 v56, v18, v18
	v_fmac_f32_e32 v57, v20, v20
	v_add_f32_e32 v56, v56, v57
	v_add_f32_e32 v1, v1, v56
	s_waitcnt vmcnt(3)
	v_mul_f32_e32 v56, v15, v15
	v_mul_f32_e32 v57, v17, v17
	v_fmac_f32_e32 v56, v14, v14
	v_fmac_f32_e32 v57, v16, v16
	v_add_f32_e32 v56, v56, v57
	v_add_f32_e32 v1, v1, v56
	s_waitcnt vmcnt(2)
	v_mul_f32_e32 v56, v11, v11
	v_mul_f32_e32 v57, v13, v13
	v_fmac_f32_e32 v56, v10, v10
	v_fmac_f32_e32 v57, v12, v12
	v_add_f32_e32 v56, v56, v57
	v_add_f32_e32 v1, v1, v56
	s_waitcnt vmcnt(1)
	v_mul_f32_e32 v56, v7, v7
	v_mul_f32_e32 v57, v9, v9
	v_fmac_f32_e32 v56, v6, v6
	v_fmac_f32_e32 v57, v8, v8
	v_add_f32_e32 v56, v56, v57
	v_add_f32_e32 v1, v1, v56
	s_waitcnt vmcnt(0)
	v_mul_f32_e32 v56, v3, v3
	v_mul_f32_e32 v57, v5, v5
	v_fmac_f32_e32 v56, v2, v2
	v_fmac_f32_e32 v57, v4, v4
	v_add_f32_e32 v56, v56, v57
	v_add_f32_e32 v1, v1, v56
	ds_bpermute_b32 v56, v50, v1
	s_waitcnt lgkmcnt(0)
	v_add_f32_e32 v1, v1, v56
	ds_bpermute_b32 v56, v51, v1
	s_waitcnt lgkmcnt(0)
	v_add_f32_e32 v1, v1, v56
	ds_bpermute_b32 v56, v52, v1
	s_waitcnt lgkmcnt(0)
	v_add_f32_e32 v1, v1, v56
	ds_bpermute_b32 v56, v53, v1
	s_waitcnt lgkmcnt(0)
	v_add_f32_e32 v1, v1, v56
	ds_bpermute_b32 v56, v54, v1
	s_waitcnt lgkmcnt(0)
	v_add_f32_e32 v1, v1, v56
	ds_bpermute_b32 v56, v55, v1
	s_waitcnt lgkmcnt(0)
; __device__ __forceinline__ unsigned pk2(float lo, float hi) { return f2bf(lo) | (f2bf(hi) << 16); }
; __device__ __forceinline__ float rms_row_load(const float* xrow, int lane, f32x4 (&v)[8]) {
;     ...
;     return 1.0f / sqrtf(wave_sum(s) * (1.0f / D) + EPS);
; }
; __device__ __forceinline__ void rms_row_to_bf16(const float* xrow, const float* gain, bf16* orow, int lane) {
;     f32x4 v[8]; const float rstd = rms_row_load(xrow, lane, v);
;     const f32x4* gr = (const f32x4*)gain + lane; unsigned long long* o8 = (unsigned long long*)orow + lane;
; #pragma unroll
;     for (int j = 0; j < 8; ++j) { const f32x4 g = gr[64 * j]; o8[64 * j] = (unsigned long long)pk2(v[j].x * rstd * g.x, v[j].y * rstd * g.y) | ((unsigned long long)pk2(v[j].z * rstd * g.z, v[j].w * rstd * g.w) << 32); }
	v_add_f32_e32 v1, v1, v56
	v_fmamk_f32 v1, v1, 0x3a000000, v226
	v_cmp_gt_f32_e32 vcc, s5, v1
	v_mul_f32_e32 v92, 0x4f800000, v1
	s_nop 0
	v_cndmask_b32_e32 v1, v1, v92, vcc
	v_sqrt_f32_e32 v92, v1
	s_nop 0
	v_add_u32_e32 v93, -1, v92
	v_fma_f32 v56, -v93, v92, v1
	v_cmp_ge_f32_e64 s[0:1], 0, v56
	v_add_u32_e32 v56, 1, v92
	s_nop 0
	v_cndmask_b32_e64 v93, v92, v93, s[0:1]
	v_fma_f32 v92, -v56, v92, v1
	v_cmp_lt_f32_e64 s[0:1], 0, v92
	s_nop 1
	v_cndmask_b32_e64 v92, v93, v56, s[0:1]
	v_mul_f32_e32 v93, 0x37800000, v92
	v_cndmask_b32_e32 v92, v92, v93, vcc
	v_cmp_class_f32_e32 vcc, v1, v225
	s_nop 1
	v_cndmask_b32_e32 v1, v92, v1, vcc
	v_div_scale_f32 v92, s[0:1], v1, v1, 1.0
	v_rcp_f32_e32 v93, v92
	s_nop 0
	v_fma_f32 v56, -v92, v93, 1.0
	v_fmac_f32_e32 v93, v56, v93
	v_div_scale_f32 v56, vcc, 1.0, v1, 1.0
	v_mul_f32_e32 v57, v56, v93
	v_fma_f32 v58, -v92, v57, v56
	v_fmac_f32_e32 v57, v58, v93
	v_fma_f32 v92, -v92, v57, v56
	v_div_fmas_f32 v92, v92, v93, v57
	v_div_fixup_f32 v1, v92, v1, 1.0
	v_mul_f32_e32 v30, v30, v1
	v_mul_f32_e32 v31, v31, v1
	v_mul_f32_e32 v32, v32, v1
	v_mul_f32_e32 v33, v33, v1
	v_mul_f32_e32 v30, v60, v30
	v_mul_f32_e32 v31, v61, v31
	v_mul_f32_e32 v32, v62, v32
	v_mul_f32_e32 v33, v63, v33
	v_bfe_u32 v56, v30, 16, 1
	v_bfe_u32 v57, v31, 16, 1
	v_bfe_u32 v58, v32, 16, 1
	v_bfe_u32 v59, v33, 16, 1
	v_add3_u32 v30, v30, v56, s36
	v_add3_u32 v31, v31, v57, s36
	v_add3_u32 v32, v32, v58, s36
	v_add3_u32 v33, v33, v59, s36
	v_lshrrev_b32_e32 v30, 16, v30
	v_lshrrev_b32_e32 v32, 16, v32
	v_and_or_b32 v30, v31, s27, v30
	v_and_or_b32 v31, v33, s27, v32
	global_store_dwordx2 v[48:49], v[30:31], off
	v_mul_f32_e32 v26, v26, v1
	v_mul_f32_e32 v27, v27, v1
	v_mul_f32_e32 v28, v28, v1
	v_mul_f32_e32 v29, v29, v1
	v_mul_f32_e32 v26, v64, v26
	v_mul_f32_e32 v27, v65, v27
	v_mul_f32_e32 v28, v66, v28
	v_mul_f32_e32 v29, v67, v29
	v_bfe_u32 v56, v26, 16, 1
	v_bfe_u32 v57, v27, 16, 1
	v_bfe_u32 v58, v28, 16, 1
	v_bfe_u32 v59, v29, 16, 1
	v_add3_u32 v26, v26, v56, s36
	v_add3_u32 v27, v27, v57, s36
	v_add3_u32 v28, v28, v58, s36
	v_add3_u32 v29, v29, v59, s36
	v_lshrrev_b32_e32 v26, 16, v26
	v_lshrrev_b32_e32 v28, 16, v28
	v_and_or_b32 v26, v27, s27, v26
	v_and_or_b32 v27, v29, s27, v28
	global_store_dwordx2 v[48:49], v[26:27], off offset:512
	v_mul_f32_e32 v22, v22, v1
	v_mul_f32_e32 v23, v23, v1
	v_mul_f32_e32 v24, v24, v1
	v_mul_f32_e32 v25, v25, v1
	v_mul_f32_e32 v22, v68, v22
	v_mul_f32_e32 v23, v69, v23
	v_mul_f32_e32 v24, v70, v24
	v_mul_f32_e32 v25, v71, v25
	v_bfe_u32 v56, v22, 16, 1
	v_bfe_u32 v57, v23, 16, 1
	v_bfe_u32 v58, v24, 16, 1
	v_bfe_u32 v59, v25, 16, 1
	v_add3_u32 v22, v22, v56, s36
	v_add3_u32 v23, v23, v57, s36
	v_add3_u32 v24, v24, v58, s36
	v_add3_u32 v25, v25, v59, s36
	v_lshrrev_b32_e32 v22, 16, v22
	v_lshrrev_b32_e32 v24, 16, v24
	v_and_or_b32 v22, v23, s27, v22
	v_and_or_b32 v23, v25, s27, v24
	global_store_dwordx2 v[48:49], v[22:23], off offset:1024
	v_mul_f32_e32 v18, v18, v1
	v_mul_f32_e32 v19, v19, v1
	v_mul_f32_e32 v20, v20, v1
	v_mul_f32_e32 v21, v21, v1
	v_mul_f32_e32 v18, v72, v18
	v_mul_f32_e32 v19, v73, v19
	v_mul_f32_e32 v20, v74, v20
	v_mul_f32_e32 v21, v75, v21
	v_bfe_u32 v56, v18, 16, 1
	v_bfe_u32 v57, v19, 16, 1
	v_bfe_u32 v58, v20, 16, 1
	v_bfe_u32 v59, v21, 16, 1
	v_add3_u32 v18, v18, v56, s36
	v_add3_u32 v19, v19, v57, s36
	v_add3_u32 v20, v20, v58, s36
	v_add3_u32 v21, v21, v59, s36
	v_lshrrev_b32_e32 v18, 16, v18
	v_lshrrev_b32_e32 v20, 16, v20
	v_and_or_b32 v18, v19, s27, v18
	v_and_or_b32 v19, v21, s27, v20
	global_store_dwordx2 v[48:49], v[18:19], off offset:1536
	v_mul_f32_e32 v14, v14, v1
	v_mul_f32_e32 v15, v15, v1
	v_mul_f32_e32 v16, v16, v1
	v_mul_f32_e32 v17, v17, v1
	v_mul_f32_e32 v14, v76, v14
	v_mul_f32_e32 v15, v77, v15
	v_mul_f32_e32 v16, v78, v16
	v_mul_f32_e32 v17, v79, v17
	v_bfe_u32 v56, v14, 16, 1
	v_bfe_u32 v57, v15, 16, 1
	v_bfe_u32 v58, v16, 16, 1
	v_bfe_u32 v59, v17, 16, 1
	v_add3_u32 v14, v14, v56, s36
	v_add3_u32 v15, v15, v57, s36
	v_add3_u32 v16, v16, v58, s36
	v_add3_u32 v17, v17, v59, s36
	v_lshrrev_b32_e32 v14, 16, v14
	v_lshrrev_b32_e32 v16, 16, v16
	v_and_or_b32 v14, v15, s27, v14
	v_and_or_b32 v15, v17, s27, v16
	global_store_dwordx2 v[48:49], v[14:15], off offset:2048
	v_mul_f32_e32 v10, v10, v1
	v_mul_f32_e32 v11, v11, v1
	v_mul_f32_e32 v12, v12, v1
	v_mul_f32_e32 v13, v13, v1
	v_mul_f32_e32 v10, v80, v10
	v_mul_f32_e32 v11, v81, v11
	v_mul_f32_e32 v12, v82, v12
	v_mul_f32_e32 v13, v83, v13
	v_bfe_u32 v56, v10, 16, 1
	v_bfe_u32 v57, v11, 16, 1
	v_bfe_u32 v58, v12, 16, 1
	v_bfe_u32 v59, v13, 16, 1
	v_add3_u32 v10, v10, v56, s36
	v_add3_u32 v11, v11, v57, s36
	v_add3_u32 v12, v12, v58, s36
	v_add3_u32 v13, v13, v59, s36
	v_lshrrev_b32_e32 v10, 16, v10
	v_lshrrev_b32_e32 v12, 16, v12
	v_and_or_b32 v10, v11, s27, v10
	v_and_or_b32 v11, v13, s27, v12
	global_store_dwordx2 v[48:49], v[10:11], off offset:2560
	v_mul_f32_e32 v6, v6, v1
	v_mul_f32_e32 v7, v7, v1
	v_mul_f32_e32 v8, v8, v1
	v_mul_f32_e32 v9, v9, v1
	v_mul_f32_e32 v6, v84, v6
	v_mul_f32_e32 v7, v85, v7
	v_mul_f32_e32 v8, v86, v8
	v_mul_f32_e32 v9, v87, v9
	v_bfe_u32 v56, v6, 16, 1
	v_bfe_u32 v57, v7, 16, 1
	v_bfe_u32 v58, v8, 16, 1
	v_bfe_u32 v59, v9, 16, 1
	v_add3_u32 v6, v6, v56, s36
	v_add3_u32 v7, v7, v57, s36
	v_add3_u32 v8, v8, v58, s36
	v_add3_u32 v9, v9, v59, s36
	v_lshrrev_b32_e32 v6, 16, v6
	v_lshrrev_b32_e32 v8, 16, v8
	v_and_or_b32 v6, v7, s27, v6
	v_and_or_b32 v7, v9, s27, v8
	global_store_dwordx2 v[48:49], v[6:7], off offset:3072
	v_mul_f32_e32 v2, v2, v1
	v_mul_f32_e32 v3, v3, v1
	v_mul_f32_e32 v4, v4, v1
	v_mul_f32_e32 v5, v5, v1
	v_mul_f32_e32 v2, v88, v2
	v_mul_f32_e32 v3, v89, v3
	v_mul_f32_e32 v4, v90, v4
	v_mul_f32_e32 v5, v91, v5
	v_bfe_u32 v56, v2, 16, 1
	v_bfe_u32 v57, v3, 16, 1
	v_bfe_u32 v58, v4, 16, 1
	v_bfe_u32 v59, v5, 16, 1
	v_add3_u32 v2, v2, v56, s36
	v_add3_u32 v3, v3, v57, s36
	v_add3_u32 v4, v4, v58, s36
	v_add3_u32 v5, v5, v59, s36
	v_lshrrev_b32_e32 v2, 16, v2
	v_lshrrev_b32_e32 v4, 16, v4
	v_and_or_b32 v2, v3, s27, v2
	v_and_or_b32 v3, v5, s27, v4
	global_store_dwordx2 v[48:49], v[2:3], off offset:3584
	s_cbranch_scc0 .LBB0_780

; __device__ __forceinline__ unsigned pk2(float lo, float hi) { return f2bf(lo) | (f2bf(hi) << 16); }
; __device__ __forceinline__ float rms_row_load(const float* xrow, int lane, f32x4 (&v)[8]) {
;     const f32x4* xr = (const f32x4*)xrow + lane; float s = 0.f;
; #pragma unroll
;     for (int j = 0; j < 8; ++j) { v[j] = xr[64 * j]; s += (v[j].x * v[j].x + v[j].y * v[j].y) + (v[j].z * v[j].z + v[j].w * v[j].w); }
;     return 1.0f / sqrtf(wave_sum(s) * (1.0f / D) + EPS);
; }
; __device__ __forceinline__ void rms_row_to_bf16(const float* xrow, const float* gain, bf16* orow, int lane) {
;     f32x4 v[8]; const float rstd = rms_row_load(xrow, lane, v);
;     const f32x4* gr = (const f32x4*)gain + lane; unsigned long long* o8 = (unsigned long long*)orow + lane;
; #pragma unroll
;     for (int j = 0; j < 8; ++j) { const f32x4 g = gr[64 * j]; o8[64 * j] = (unsigned long long)pk2(v[j].x * rstd * g.x, v[j].y * rstd * g.y) | ((unsigned long long)pk2(v[j].z * rstd * g.z, v[j].w * rstd * g.w) << 32); }
; }
; __global__ void __launch_bounds__(NWAVES * 64, 2) trunk_fwd(Args args) {
;     ...
;             if (layer == 0) { for (int m = gw; m < M; m += ngw) rms_row_to_bf16(XA + (size_t)m * D, args.in[I_NMIX] + D, Hb + (size_t)m * D, lane); }
.LBB0_1351:
	v_readlane_b32 s8, v254, 59
	s_andn2_b64 vcc, exec, s[4:5]
	v_readlane_b32 s4, v250, 6
	v_readlane_b32 s9, v254, 60
	v_readlane_b32 s12, v254, 57
	v_readlane_b32 s14, v254, 61
	v_readlane_b32 s5, v250, 7
	s_mov_b32 s9, 0xf800000
	s_mov_b32 s10, 0x36da2000
	s_mov_b32 s11, 0x34da1000
	v_readlane_b32 s13, v254, 58
	v_readlane_b32 s15, v254, 62
	s_cbranch_vccnz .LBB0_1355
	s_and_b64 vcc, exec, s[0:1]
	s_cbranch_vccnz .LBB0_1355
	v_and_b32_e32 v2, 64, v228
	v_add_u32_e32 v2, 64, v2
	v_xor_b32_e32 v3, 1, v228
	v_cmp_lt_i32_e32 vcc, v3, v2
	v_readlane_b32 s0, v252, 57
	v_lshlrev_b32_e32 v186, 4, v1
	v_cndmask_b32_e32 v3, v228, v3, vcc
	v_lshlrev_b32_e32 v50, 2, v3
	v_xor_b32_e32 v3, 2, v228
	v_cmp_lt_i32_e32 vcc, v3, v2
	v_readlane_b32 s1, v252, 58
	s_ashr_i32 s7, s6, 31
	v_cndmask_b32_e32 v3, v228, v3, vcc
	v_lshlrev_b32_e32 v51, 2, v3
	v_xor_b32_e32 v3, 4, v228
	v_cmp_lt_i32_e32 vcc, v3, v2
	v_lshl_add_u64 v[34:35], s[0:1], 0, v[186:187]
	s_mov_b64 s[0:1], 0x1000
	v_cndmask_b32_e32 v3, v228, v3, vcc
	v_lshlrev_b32_e32 v52, 2, v3
	v_xor_b32_e32 v3, 8, v228
	v_cmp_lt_i32_e32 vcc, v3, v2
	v_lshl_add_u64 v[36:37], v[34:35], 0, s[0:1]
	s_mov_b64 s[0:1], 0x1400
	v_cndmask_b32_e32 v3, v228, v3, vcc
	v_lshlrev_b32_e32 v53, 2, v3
	v_xor_b32_e32 v3, 16, v228
	v_cmp_lt_i32_e32 vcc, v3, v2
	v_lshl_add_u64 v[38:39], v[34:35], 0, s[0:1]
	s_mov_b64 s[0:1], 0x1800
	v_cndmask_b32_e32 v3, v228, v3, vcc
	v_lshlrev_b32_e32 v54, 2, v3
	v_xor_b32_e32 v3, 32, v228
	v_lshl_add_u64 v[40:41], v[34:35], 0, s[0:1]
	s_mov_b64 s[0:1], 0x1c00
	v_cmp_lt_i32_e32 vcc, v3, v2
	v_lshl_add_u64 v[42:43], v[34:35], 0, s[0:1]
	s_lshl_b64 s[0:1], s[6:7], 12
	v_cndmask_b32_e32 v2, v228, v3, vcc
	v_lshl_or_b32 v44, v1, 3, s0
	v_mov_b32_e32 v45, s1
	s_lshl_b64 s[0:1], s[6:7], 13
	v_lshlrev_b32_e32 v55, 2, v2
	v_or_b32_e32 v46, s0, v186
	v_mov_b32_e32 v47, s1
	global_load_dwordx4 v[60:63], v[34:35], off
	global_load_dwordx4 v[64:67], v[34:35], off offset:1024
	global_load_dwordx4 v[68:71], v[34:35], off offset:2048
	global_load_dwordx4 v[72:75], v[34:35], off offset:3072
	global_load_dwordx4 v[76:79], v[36:37], off
	global_load_dwordx4 v[80:83], v[38:39], off
	global_load_dwordx4 v[84:87], v[40:41], off
	global_load_dwordx4 v[88:91], v[42:43], off
.LBB0_1354:
	v_lshl_add_u64 v[2:3], s[4:5], 0, v[46:47]
	v_add_co_u32_e32 v4, vcc, 0x36da1000, v2
	s_add_i32 s6, s6, s8
	s_nop 0
	v_addc_co_u32_e32 v5, vcc, 0, v3, vcc
	global_load_dwordx4 v[30:33], v[4:5], off
	global_load_dwordx4 v[26:29], v[4:5], off offset:1024
	global_load_dwordx4 v[22:25], v[4:5], off offset:2048
	global_load_dwordx4 v[18:21], v[4:5], off offset:3072
	v_add_co_u32_e32 v2, vcc, s10, v2
	v_lshl_add_u64 v[46:47], v[46:47], 0, s[14:15]
	s_nop 0
	v_addc_co_u32_e32 v3, vcc, 0, v3, vcc
	global_load_dwordx4 v[14:17], v[2:3], off
	global_load_dwordx4 v[10:13], v[2:3], off offset:1024
	global_load_dwordx4 v[6:9], v[2:3], off offset:2048
	global_load_dwordx4 v[2:5], v[2:3], off offset:3072
	s_cmpk_gt_i32 s6, 0x1fff
	v_lshl_add_u64 v[48:49], s[4:5], 0, v[44:45]
	v_add_co_u32_e32 v48, vcc, s11, v48
	s_nop 1
	v_addc_co_u32_e32 v49, vcc, 0, v49, vcc
	v_lshl_add_u64 v[44:45], v[44:45], 0, s[12:13]
	s_waitcnt vmcnt(7)
	v_mul_f32_e32 v1, v31, v31
	v_mul_f32_e32 v57, v33, v33
	v_fmac_f32_e32 v1, v30, v30
	v_fmac_f32_e32 v57, v32, v32
	v_add_f32_e32 v1, v1, v57
	s_waitcnt vmcnt(6)
	v_mul_f32_e32 v56, v27, v27
	v_mul_f32_e32 v57, v29, v29
	v_fmac_f32_e32 v56, v26, v26
	v_fmac_f32_e32 v57, v28, v28
	v_add_f32_e32 v56, v56, v57
	v_add_f32_e32 v1, v1, v56
	s_waitcnt vmcnt(5)
	v_mul_f32_e32 v56, v23, v23
	v_mul_f32_e32 v57, v25, v25
	v_fmac_f32_e32 v56, v22, v22
	v_fmac_f32_e32 v57, v24, v24
	v_add_f32_e32 v56, v56, v57
	v_add_f32_e32 v1, v1, v56
	s_waitcnt vmcnt(4)
	v_mul_f32_e32 v56, v19, v19
	v_mul_f32_e32 v57, v21, v21
	v_fmac_f32_e32 v56, v18, v18
	v_fmac_f32_e32 v57, v20, v20
	v_add_f32_e32 v56, v56, v57
	v_add_f32_e32 v1, v1, v56
	s_waitcnt vmcnt(3)
	v_mul_f32_e32 v56, v15, v15
	v_mul_f32_e32 v57, v17, v17
	v_fmac_f32_e32 v56, v14, v14
	v_fmac_f32_e32 v57, v16, v16
	v_add_f32_e32 v56, v56, v57
	v_add_f32_e32 v1, v1, v56
	s_waitcnt vmcnt(2)
	v_mul_f32_e32 v56, v11, v11
	v_mul_f32_e32 v57, v13, v13
	v_fmac_f32_e32 v56, v10, v10
	v_fmac_f32_e32 v57, v12, v12
	v_add_f32_e32 v56, v56, v57
	v_add_f32_e32 v1, v1, v56
	s_waitcnt vmcnt(1)
	v_mul_f32_e32 v56, v7, v7
	v_mul_f32_e32 v57, v9, v9
	v_fmac_f32_e32 v56, v6, v6
	v_fmac_f32_e32 v57, v8, v8
	v_add_f32_e32 v56, v56, v57
	v_add_f32_e32 v1, v1, v56
	s_waitcnt vmcnt(0)
	v_mul_f32_e32 v56, v3, v3
	v_mul_f32_e32 v57, v5, v5
	v_fmac_f32_e32 v56, v2, v2
	v_fmac_f32_e32 v57, v4, v4
	v_add_f32_e32 v56, v56, v57
	v_add_f32_e32 v1, v1, v56
	ds_bpermute_b32 v56, v50, v1
	s_waitcnt lgkmcnt(0)
	v_add_f32_e32 v1, v1, v56
	ds_bpermute_b32 v56, v51, v1
	s_waitcnt lgkmcnt(0)
	v_add_f32_e32 v1, v1, v56
	ds_bpermute_b32 v56, v52, v1
	s_waitcnt lgkmcnt(0)
	v_add_f32_e32 v1, v1, v56
	ds_bpermute_b32 v56, v53, v1
	s_waitcnt lgkmcnt(0)
	v_add_f32_e32 v1, v1, v56
	ds_bpermute_b32 v56, v54, v1
	s_waitcnt lgkmcnt(0)
	v_add_f32_e32 v1, v1, v56
	ds_bpermute_b32 v56, v55, v1
	s_waitcnt lgkmcnt(0)
; __device__ __forceinline__ unsigned pk2(float lo, float hi) { return f2bf(lo) | (f2bf(hi) << 16); }
; __device__ __forceinline__ float rms_row_load(const float* xrow, int lane, f32x4 (&v)[8]) {
;     ...
;     return 1.0f / sqrtf(wave_sum(s) * (1.0f / D) + EPS);
; }
; __device__ __forceinline__ void rms_row_to_bf16(const float* xrow, const float* gain, bf16* orow, int lane) {
;     f32x4 v[8]; const float rstd = rms_row_load(xrow, lane, v);
;     const f32x4* gr = (const f32x4*)gain + lane; unsigned long long* o8 = (unsigned long long*)orow + lane;
; #pragma unroll
;     for (int j = 0; j < 8; ++j) { const f32x4 g = gr[64 * j]; o8[64 * j] = (unsigned long long)pk2(v[j].x * rstd * g.x, v[j].y * rstd * g.y) | ((unsigned long long)pk2(v[j].z * rstd * g.z, v[j].w * rstd * g.w) << 32); }
	v_add_f32_e32 v1, v1, v56
	v_fmamk_f32 v1, v1, 0x3a000000, v226
	v_cmp_gt_f32_e32 vcc, s9, v1
	v_mul_f32_e32 v92, 0x4f800000, v1
	s_nop 0
	v_cndmask_b32_e32 v1, v1, v92, vcc
	v_sqrt_f32_e32 v92, v1
	s_nop 0
	v_add_u32_e32 v93, -1, v92
	v_fma_f32 v56, -v93, v92, v1
	v_cmp_ge_f32_e64 s[0:1], 0, v56
	v_add_u32_e32 v56, 1, v92
	s_nop 0
	v_cndmask_b32_e64 v93, v92, v93, s[0:1]
	v_fma_f32 v92, -v56, v92, v1
	v_cmp_lt_f32_e64 s[0:1], 0, v92
	s_nop 1
	v_cndmask_b32_e64 v92, v93, v56, s[0:1]
	v_mul_f32_e32 v93, 0x37800000, v92
	v_cndmask_b32_e32 v92, v92, v93, vcc
	v_cmp_class_f32_e32 vcc, v1, v225
	s_nop 1
	v_cndmask_b32_e32 v1, v92, v1, vcc
	v_div_scale_f32 v92, s[0:1], v1, v1, 1.0
	v_rcp_f32_e32 v93, v92
	s_nop 0
	v_fma_f32 v56, -v92, v93, 1.0
	v_fmac_f32_e32 v93, v56, v93
	v_div_scale_f32 v56, vcc, 1.0, v1, 1.0
	v_mul_f32_e32 v57, v56, v93
	v_fma_f32 v58, -v92, v57, v56
	v_fmac_f32_e32 v57, v58, v93
	v_fma_f32 v92, -v92, v57, v56
	v_div_fmas_f32 v92, v92, v93, v57
	v_div_fixup_f32 v1, v92, v1, 1.0
	v_mul_f32_e32 v30, v30, v1
	v_mul_f32_e32 v31, v31, v1
	v_mul_f32_e32 v32, v32, v1
	v_mul_f32_e32 v33, v33, v1
	v_mul_f32_e32 v30, v60, v30
	v_mul_f32_e32 v31, v61, v31
	v_mul_f32_e32 v32, v62, v32
	v_mul_f32_e32 v33, v63, v33
	v_bfe_u32 v56, v30, 16, 1
	v_bfe_u32 v57, v31, 16, 1
	v_bfe_u32 v58, v32, 16, 1
	v_bfe_u32 v59, v33, 16, 1
	v_add3_u32 v30, v30, v56, s36
	v_add3_u32 v31, v31, v57, s36
	v_add3_u32 v32, v32, v58, s36
	v_add3_u32 v33, v33, v59, s36
	v_lshrrev_b32_e32 v30, 16, v30
	v_lshrrev_b32_e32 v32, 16, v32
	v_and_or_b32 v30, v31, s27, v30
	v_and_or_b32 v31, v33, s27, v32
	global_store_dwordx2 v[48:49], v[30:31], off
	v_mul_f32_e32 v26, v26, v1
	v_mul_f32_e32 v27, v27, v1
	v_mul_f32_e32 v28, v28, v1
	v_mul_f32_e32 v29, v29, v1
	v_mul_f32_e32 v26, v64, v26
	v_mul_f32_e32 v27, v65, v27
	v_mul_f32_e32 v28, v66, v28
	v_mul_f32_e32 v29, v67, v29
	v_bfe_u32 v56, v26, 16, 1
	v_bfe_u32 v57, v27, 16, 1
	v_bfe_u32 v58, v28, 16, 1
	v_bfe_u32 v59, v29, 16, 1
	v_add3_u32 v26, v26, v56, s36
	v_add3_u32 v27, v27, v57, s36
	v_add3_u32 v28, v28, v58, s36
	v_add3_u32 v29, v29, v59, s36
	v_lshrrev_b32_e32 v26, 16, v26
	v_lshrrev_b32_e32 v28, 16, v28
	v_and_or_b32 v26, v27, s27, v26
	v_and_or_b32 v27, v29, s27, v28
	global_store_dwordx2 v[48:49], v[26:27], off offset:512
	v_mul_f32_e32 v22, v22, v1
	v_mul_f32_e32 v23, v23, v1
	v_mul_f32_e32 v24, v24, v1
	v_mul_f32_e32 v25, v25, v1
	v_mul_f32_e32 v22, v68, v22
	v_mul_f32_e32 v23, v69, v23
	v_mul_f32_e32 v24, v70, v24
	v_mul_f32_e32 v25, v71, v25
	v_bfe_u32 v56, v22, 16, 1
	v_bfe_u32 v57, v23, 16, 1
	v_bfe_u32 v58, v24, 16, 1
	v_bfe_u32 v59, v25, 16, 1
	v_add3_u32 v22, v22, v56, s36
	v_add3_u32 v23, v23, v57, s36
	v_add3_u32 v24, v24, v58, s36
	v_add3_u32 v25, v25, v59, s36
	v_lshrrev_b32_e32 v22, 16, v22
	v_lshrrev_b32_e32 v24, 16, v24
	v_and_or_b32 v22, v23, s27, v22
	v_and_or_b32 v23, v25, s27, v24
	global_store_dwordx2 v[48:49], v[22:23], off offset:1024
	v_mul_f32_e32 v18, v18, v1
	v_mul_f32_e32 v19, v19, v1
	v_mul_f32_e32 v20, v20, v1
	v_mul_f32_e32 v21, v21, v1
	v_mul_f32_e32 v18, v72, v18
	v_mul_f32_e32 v19, v73, v19
	v_mul_f32_e32 v20, v74, v20
	v_mul_f32_e32 v21, v75, v21
	v_bfe_u32 v56, v18, 16, 1
	v_bfe_u32 v57, v19, 16, 1
	v_bfe_u32 v58, v20, 16, 1
	v_bfe_u32 v59, v21, 16, 1
	v_add3_u32 v18, v18, v56, s36
	v_add3_u32 v19, v19, v57, s36
	v_add3_u32 v20, v20, v58, s36
	v_add3_u32 v21, v21, v59, s36
	v_lshrrev_b32_e32 v18, 16, v18
	v_lshrrev_b32_e32 v20, 16, v20
	v_and_or_b32 v18, v19, s27, v18
	v_and_or_b32 v19, v21, s27, v20
	global_store_dwordx2 v[48:49], v[18:19], off offset:1536
	v_mul_f32_e32 v14, v14, v1
	v_mul_f32_e32 v15, v15, v1
	v_mul_f32_e32 v16, v16, v1
	v_mul_f32_e32 v17, v17, v1
	v_mul_f32_e32 v14, v76, v14
	v_mul_f32_e32 v15, v77, v15
	v_mul_f32_e32 v16, v78, v16
	v_mul_f32_e32 v17, v79, v17
	v_bfe_u32 v56, v14, 16, 1
	v_bfe_u32 v57, v15, 16, 1
	v_bfe_u32 v58, v16, 16, 1
	v_bfe_u32 v59, v17, 16, 1
	v_add3_u32 v14, v14, v56, s36
	v_add3_u32 v15, v15, v57, s36
	v_add3_u32 v16, v16, v58, s36
	v_add3_u32 v17, v17, v59, s36
	v_lshrrev_b32_e32 v14, 16, v14
	v_lshrrev_b32_e32 v16, 16, v16
	v_and_or_b32 v14, v15, s27, v14
	v_and_or_b32 v15, v17, s27, v16
	global_store_dwordx2 v[48:49], v[14:15], off offset:2048
	v_mul_f32_e32 v10, v10, v1
	v_mul_f32_e32 v11, v11, v1
	v_mul_f32_e32 v12, v12, v1
	v_mul_f32_e32 v13, v13, v1
	v_mul_f32_e32 v10, v80, v10
	v_mul_f32_e32 v11, v81, v11
	v_mul_f32_e32 v12, v82, v12
	v_mul_f32_e32 v13, v83, v13
	v_bfe_u32 v56, v10, 16, 1
	v_bfe_u32 v57, v11, 16, 1
	v_bfe_u32 v58, v12, 16, 1
	v_bfe_u32 v59, v13, 16, 1
	v_add3_u32 v10, v10, v56, s36
	v_add3_u32 v11, v11, v57, s36
	v_add3_u32 v12, v12, v58, s36
	v_add3_u32 v13, v13, v59, s36
	v_lshrrev_b32_e32 v10, 16, v10
	v_lshrrev_b32_e32 v12, 16, v12
	v_and_or_b32 v10, v11, s27, v10
	v_and_or_b32 v11, v13, s27, v12
	global_store_dwordx2 v[48:49], v[10:11], off offset:2560
	v_mul_f32_e32 v6, v6, v1
	v_mul_f32_e32 v7, v7, v1
	v_mul_f32_e32 v8, v8, v1
	v_mul_f32_e32 v9, v9, v1
	v_mul_f32_e32 v6, v84, v6
	v_mul_f32_e32 v7, v85, v7
	v_mul_f32_e32 v8, v86, v8
	v_mul_f32_e32 v9, v87, v9
	v_bfe_u32 v56, v6, 16, 1
	v_bfe_u32 v57, v7, 16, 1
	v_bfe_u32 v58, v8, 16, 1
	v_bfe_u32 v59, v9, 16, 1
	v_add3_u32 v6, v6, v56, s36
	v_add3_u32 v7, v7, v57, s36
	v_add3_u32 v8, v8, v58, s36
	v_add3_u32 v9, v9, v59, s36
	v_lshrrev_b32_e32 v6, 16, v6
	v_lshrrev_b32_e32 v8, 16, v8
	v_and_or_b32 v6, v7, s27, v6
	v_and_or_b32 v7, v9, s27, v8
	global_store_dwordx2 v[48:49], v[6:7], off offset:3072
	v_mul_f32_e32 v2, v2, v1
	v_mul_f32_e32 v3, v3, v1
	v_mul_f32_e32 v4, v4, v1
	v_mul_f32_e32 v5, v5, v1
	v_mul_f32_e32 v2, v88, v2
	v_mul_f32_e32 v3, v89, v3
	v_mul_f32_e32 v4, v90, v4
	v_mul_f32_e32 v5, v91, v5
	v_bfe_u32 v56, v2, 16, 1
	v_bfe_u32 v57, v3, 16, 1
	v_bfe_u32 v58, v4, 16, 1
	v_bfe_u32 v59, v5, 16, 1
	v_add3_u32 v2, v2, v56, s36
	v_add3_u32 v3, v3, v57, s36
	v_add3_u32 v4, v4, v58, s36
	v_add3_u32 v5, v5, v59, s36
	v_lshrrev_b32_e32 v2, 16, v2
	v_lshrrev_b32_e32 v4, 16, v4
	v_and_or_b32 v2, v3, s27, v2
	v_and_or_b32 v3, v5, s27, v4
	global_store_dwordx2 v[48:49], v[2:3], off offset:3584
	s_cbranch_scc0 .LBB0_1354
